# v049 + grid barrier: non-leader workgroups poll the global TOP counter directly (skips the per-XCD generation hop)
# baseline (speedup 1.0000x reference)
; __device__ __forceinline__ unsigned xb_ld(unsigned* p)              { return __hip_atomic_load(p, __ATOMIC_RELAXED, __HIP_MEMORY_SCOPE_AGENT); }
; __device__ __forceinline__ unsigned xb_add(unsigned* p, unsigned v) { return __hip_atomic_fetch_add(p, v, __ATOMIC_RELAXED, __HIP_MEMORY_SCOPE_AGENT); }
; #define XB_SPIN(cond, bar) do { unsigned _sp = 0; while (cond) { __builtin_amdgcn_s_sleep(1); \
;     if ((++_sp & 255u) == 0u) { if (xb_ld(&(bar)[XB_TMO])) break; if (_sp > XB_SPIN_CAP) { atomicAdd(&(bar)[XB_TMO], 1u); break; } } } } while (0)
; __device__ __forceinline__ void xcd_barrier(const XcdBarrier& b) {
;     ...
;         const unsigned old = xb_add(&bar[XB_XSUB(b.x)], 1u);
;         const unsigned gen = old / nloc;
;         if (old + 1u == (gen + 1u) * nloc) {
;     ...
;         } else {
;             XB_SPIN(xb_ld(&bar[XB_XGEN(b.x)]) == gen, bar);
;             __builtin_amdgcn_fence(__ATOMIC_ACQUIRE, "agent");
.LBB0_80:
	s_or_b64 exec, exec, s[10:11]
	v_cvt_f32_u32_e32 v5, v3
	s_waitcnt vmcnt(0)
	v_readfirstlane_b32 s3, v4
	v_sub_u32_e32 v4, 0, v3
	v_rcp_iflag_f32_e32 v5, v5
	v_add_u32_e32 v6, s3, v2
	v_mul_f32_e32 v5, 0x4f7ffffe, v5
	v_cvt_u32_f32_e32 v5, v5
	v_mul_lo_u32 v2, v4, v5
	v_mul_hi_u32 v2, v5, v2
	v_add_u32_e32 v2, v5, v2
	v_mul_hi_u32 v2, v6, v2
	v_mul_lo_u32 v4, v2, v3
	v_sub_u32_e32 v4, v6, v4
	v_add_u32_e32 v5, 1, v2
	v_cmp_ge_u32_e32 vcc, v4, v3
	s_nop 1
	v_cndmask_b32_e32 v2, v2, v5, vcc
	v_sub_u32_e32 v5, v4, v3
	v_cndmask_b32_e32 v4, v4, v5, vcc
	v_add_u32_e32 v5, 1, v2
	v_cmp_ge_u32_e32 vcc, v4, v3
	v_add_u32_e32 v4, 1, v6
	s_nop 0
	v_cndmask_b32_e32 v2, v2, v5, vcc
	v_mul_lo_u32 v5, v3, v2
	v_add_u32_e32 v3, v5, v3
	v_cmp_ne_u32_e32 vcc, v4, v3
	s_and_saveexec_b64 s[8:9], vcc
	s_xor_b64 s[8:9], exec, s[8:9]
	s_cbranch_execz .LBB0_94
	s_waitcnt lgkmcnt(0)
	buffer_inv sc1
	v_add_u32_e32 v7, 1, v2
	v_mul_lo_u32 v7, v7, v1
	v_mov_b32_e32 v8, 0x3400
	v_mov_b32_e32 v1, 0x2000
	global_load_dword v1, v8, s[90:91] sc1
	s_add_u32 s12, s6, 0x2400
	s_addc_u32 s13, s7, 0
	s_waitcnt vmcnt(0)
	v_cmp_lt_u32_e32 vcc, v1, v7
	s_and_saveexec_b64 s[10:11], vcc
	s_cbranch_execz .LBB0_93
	s_mov_b32 s3, 1
	s_mov_b64 s[14:15], 0
	v_mov_b32_e32 v1, 0
	s_branch .LBB0_84

; __device__ __forceinline__ unsigned xb_ld(unsigned* p)              { return __hip_atomic_load(p, __ATOMIC_RELAXED, __HIP_MEMORY_SCOPE_AGENT); }
; #define XB_SPIN(cond, bar) do { unsigned _sp = 0; while (cond) { __builtin_amdgcn_s_sleep(1); \
;     if ((++_sp & 255u) == 0u) { if (xb_ld(&(bar)[XB_TMO])) break; if (_sp > XB_SPIN_CAP) { atomicAdd(&(bar)[XB_TMO], 1u); break; } } } } while (0)
; __device__ __forceinline__ void xcd_barrier(const XcdBarrier& b) {
;     ...
;             XB_SPIN(xb_ld(&bar[XB_XGEN(b.x)]) == gen, bar);
.LBB0_86:
	global_load_dword v3, v8, s[90:91] sc1
	s_add_i32 s3, s3, 1
	s_mov_b64 s[20:21], -1
	s_waitcnt vmcnt(0)
	v_cmp_ge_u32_e32 vcc, v3, v7
	s_orn2_b64 s[18:19], vcc, exec
	s_branch .LBB0_83

; __device__ __forceinline__ unsigned xb_ld(unsigned* p)              { return __hip_atomic_load(p, __ATOMIC_RELAXED, __HIP_MEMORY_SCOPE_AGENT); }
; __device__ __forceinline__ unsigned xb_add(unsigned* p, unsigned v) { return __hip_atomic_fetch_add(p, v, __ATOMIC_RELAXED, __HIP_MEMORY_SCOPE_AGENT); }
; #define XB_SPIN(cond, bar) do { unsigned _sp = 0; while (cond) { __builtin_amdgcn_s_sleep(1); \
;     if ((++_sp & 255u) == 0u) { if (xb_ld(&(bar)[XB_TMO])) break; if (_sp > XB_SPIN_CAP) { atomicAdd(&(bar)[XB_TMO], 1u); break; } } } } while (0)
; __device__ __forceinline__ void xcd_barrier(const XcdBarrier& b) {
;     ...
;         const unsigned old = xb_add(&bar[XB_XSUB(b.x)], 1u);
;         const unsigned gen = old / nloc;
;         if (old + 1u == (gen + 1u) * nloc) {
;     ...
;         } else {
;             XB_SPIN(xb_ld(&bar[XB_XGEN(b.x)]) == gen, bar);
;             __builtin_amdgcn_fence(__ATOMIC_ACQUIRE, "agent");
.LBB0_141:
	s_or_b64 exec, exec, s[6:7]
	v_cvt_f32_u32_e32 v5, v3
	s_waitcnt vmcnt(0)
	v_readfirstlane_b32 s4, v4
	v_sub_u32_e32 v4, 0, v3
	v_rcp_iflag_f32_e32 v5, v5
	v_add_u32_e32 v6, s4, v2
	v_mul_f32_e32 v5, 0x4f7ffffe, v5
	v_cvt_u32_f32_e32 v5, v5
	v_mul_lo_u32 v2, v4, v5
	v_mul_hi_u32 v2, v5, v2
	v_add_u32_e32 v2, v5, v2
	v_mul_hi_u32 v2, v6, v2
	v_mul_lo_u32 v4, v2, v3
	v_sub_u32_e32 v4, v6, v4
	v_add_u32_e32 v5, 1, v2
	v_cmp_ge_u32_e32 vcc, v4, v3
	s_nop 1
	v_cndmask_b32_e32 v2, v2, v5, vcc
	v_sub_u32_e32 v5, v4, v3
	v_cndmask_b32_e32 v4, v4, v5, vcc
	v_add_u32_e32 v5, 1, v2
	v_cmp_ge_u32_e32 vcc, v4, v3
	v_add_u32_e32 v4, 1, v6
	s_nop 0
	v_cndmask_b32_e32 v2, v2, v5, vcc
	v_mul_lo_u32 v5, v3, v2
	v_add_u32_e32 v3, v5, v3
	v_cmp_ne_u32_e32 vcc, v4, v3
	s_and_saveexec_b64 s[4:5], vcc
	s_xor_b64 s[4:5], exec, s[4:5]
	s_cbranch_execz .LBB0_155
	s_waitcnt lgkmcnt(0)
	buffer_inv sc1
	v_add_u32_e32 v7, 1, v2
	v_mul_lo_u32 v7, v7, v1
	v_mov_b32_e32 v8, 0x3400
	v_mov_b32_e32 v1, 0x2000
	global_load_dword v1, v8, s[90:91] sc1
	s_add_u32 s8, s2, 0x2400
	s_addc_u32 s9, s3, 0
	s_waitcnt vmcnt(0)
	v_cmp_lt_u32_e32 vcc, v1, v7
	s_and_saveexec_b64 s[6:7], vcc
	s_cbranch_execz .LBB0_154
	s_mov_b32 s22, 1
	s_mov_b64 s[12:13], 0
	v_mov_b32_e32 v1, 0
	s_branch .LBB0_145

; __device__ __forceinline__ unsigned xb_ld(unsigned* p)              { return __hip_atomic_load(p, __ATOMIC_RELAXED, __HIP_MEMORY_SCOPE_AGENT); }
; #define XB_SPIN(cond, bar) do { unsigned _sp = 0; while (cond) { __builtin_amdgcn_s_sleep(1); \
;     if ((++_sp & 255u) == 0u) { if (xb_ld(&(bar)[XB_TMO])) break; if (_sp > XB_SPIN_CAP) { atomicAdd(&(bar)[XB_TMO], 1u); break; } } } } while (0)
; __device__ __forceinline__ void xcd_barrier(const XcdBarrier& b) {
;     ...
;             XB_SPIN(xb_ld(&bar[XB_XGEN(b.x)]) == gen, bar);
.LBB0_147:
	global_load_dword v3, v8, s[90:91] sc1
	s_add_i32 s22, s22, 1
	s_mov_b64 s[18:19], -1
	s_waitcnt vmcnt(0)
	v_cmp_ge_u32_e32 vcc, v3, v7
	s_orn2_b64 s[16:17], vcc, exec
	s_branch .LBB0_144

; __device__ __forceinline__ unsigned xb_ld(unsigned* p)              { return __hip_atomic_load(p, __ATOMIC_RELAXED, __HIP_MEMORY_SCOPE_AGENT); }
; __device__ __forceinline__ unsigned xb_add(unsigned* p, unsigned v) { return __hip_atomic_fetch_add(p, v, __ATOMIC_RELAXED, __HIP_MEMORY_SCOPE_AGENT); }
; #define XB_SPIN(cond, bar) do { unsigned _sp = 0; while (cond) { __builtin_amdgcn_s_sleep(1); \
;     if ((++_sp & 255u) == 0u) { if (xb_ld(&(bar)[XB_TMO])) break; if (_sp > XB_SPIN_CAP) { atomicAdd(&(bar)[XB_TMO], 1u); break; } } } } while (0)
; __device__ __forceinline__ void xcd_barrier(const XcdBarrier& b) {
;     ...
;         const unsigned old = xb_add(&bar[XB_XSUB(b.x)], 1u);
;         const unsigned gen = old / nloc;
;         if (old + 1u == (gen + 1u) * nloc) {
;     ...
;         } else {
;             XB_SPIN(xb_ld(&bar[XB_XGEN(b.x)]) == gen, bar);
;             __builtin_amdgcn_fence(__ATOMIC_ACQUIRE, "agent");
.LBB0_241:
	s_or_b64 exec, exec, s[14:15]
	v_cvt_f32_u32_e32 v5, v3
	s_waitcnt vmcnt(0)
	v_readfirstlane_b32 s12, v4
	v_sub_u32_e32 v4, 0, v3
	v_rcp_iflag_f32_e32 v5, v5
	v_add_u32_e32 v6, s12, v2
	v_mul_f32_e32 v5, 0x4f7ffffe, v5
	v_cvt_u32_f32_e32 v5, v5
	v_mul_lo_u32 v2, v4, v5
	v_mul_hi_u32 v2, v5, v2
	v_add_u32_e32 v2, v5, v2
	v_mul_hi_u32 v2, v6, v2
	v_mul_lo_u32 v4, v2, v3
	v_sub_u32_e32 v4, v6, v4
	v_add_u32_e32 v5, 1, v2
	v_cmp_ge_u32_e32 vcc, v4, v3
	s_nop 1
	v_cndmask_b32_e32 v2, v2, v5, vcc
	v_sub_u32_e32 v5, v4, v3
	v_cndmask_b32_e32 v4, v4, v5, vcc
	v_add_u32_e32 v5, 1, v2
	v_cmp_ge_u32_e32 vcc, v4, v3
	v_add_u32_e32 v4, 1, v6
	s_nop 0
	v_cndmask_b32_e32 v2, v2, v5, vcc
	v_mul_lo_u32 v5, v3, v2
	v_add_u32_e32 v3, v5, v3
	v_cmp_ne_u32_e32 vcc, v4, v3
	s_and_saveexec_b64 s[12:13], vcc
	s_xor_b64 s[12:13], exec, s[12:13]
	s_cbranch_execz .LBB0_255
	s_waitcnt lgkmcnt(0)
	buffer_inv sc1
	v_add_u32_e32 v7, 1, v2
	v_mul_lo_u32 v7, v7, v1
	v_mov_b32_e32 v8, 0x3400
	v_mov_b32_e32 v1, 0x2000
	global_load_dword v1, v8, s[90:91] sc1
	s_add_u32 s16, s4, 0x2400
	s_addc_u32 s17, s5, 0
	s_waitcnt vmcnt(0)
	v_cmp_lt_u32_e32 vcc, v1, v7
	s_and_saveexec_b64 s[14:15], vcc
	s_cbranch_execz .LBB0_254
	s_mov_b32 s28, 1
	s_mov_b64 s[18:19], 0
	v_mov_b32_e32 v1, 0
	s_branch .LBB0_245

; __device__ __forceinline__ unsigned xb_ld(unsigned* p)              { return __hip_atomic_load(p, __ATOMIC_RELAXED, __HIP_MEMORY_SCOPE_AGENT); }
; #define XB_SPIN(cond, bar) do { unsigned _sp = 0; while (cond) { __builtin_amdgcn_s_sleep(1); \
;     if ((++_sp & 255u) == 0u) { if (xb_ld(&(bar)[XB_TMO])) break; if (_sp > XB_SPIN_CAP) { atomicAdd(&(bar)[XB_TMO], 1u); break; } } } } while (0)
; __device__ __forceinline__ void xcd_barrier(const XcdBarrier& b) {
;     ...
;             XB_SPIN(xb_ld(&bar[XB_XGEN(b.x)]) == gen, bar);
.LBB0_247:
	global_load_dword v3, v8, s[90:91] sc1
	s_add_i32 s28, s28, 1
	s_mov_b64 s[24:25], -1
	s_waitcnt vmcnt(0)
	v_cmp_ge_u32_e32 vcc, v3, v7
	s_orn2_b64 s[22:23], vcc, exec
	s_branch .LBB0_244

; __device__ __forceinline__ unsigned xb_ld(unsigned* p)              { return __hip_atomic_load(p, __ATOMIC_RELAXED, __HIP_MEMORY_SCOPE_AGENT); }
; __device__ __forceinline__ unsigned xb_add(unsigned* p, unsigned v) { return __hip_atomic_fetch_add(p, v, __ATOMIC_RELAXED, __HIP_MEMORY_SCOPE_AGENT); }
; #define XB_SPIN(cond, bar) do { unsigned _sp = 0; while (cond) { __builtin_amdgcn_s_sleep(1); \
;     if ((++_sp & 255u) == 0u) { if (xb_ld(&(bar)[XB_TMO])) break; if (_sp > XB_SPIN_CAP) { atomicAdd(&(bar)[XB_TMO], 1u); break; } } } } while (0)
; __device__ __forceinline__ void xcd_barrier(const XcdBarrier& b) {
;     ...
;         const unsigned old = xb_add(&bar[XB_XSUB(b.x)], 1u);
;         const unsigned gen = old / nloc;
;         if (old + 1u == (gen + 1u) * nloc) {
;     ...
;         } else {
;             XB_SPIN(xb_ld(&bar[XB_XGEN(b.x)]) == gen, bar);
;             __builtin_amdgcn_fence(__ATOMIC_ACQUIRE, "agent");
.LBB0_661:
	s_or_b64 exec, exec, s[6:7]
	v_cvt_f32_u32_e32 v5, v3
	s_waitcnt vmcnt(0)
	v_readfirstlane_b32 s4, v4
	v_sub_u32_e32 v4, 0, v3
	v_rcp_iflag_f32_e32 v5, v5
	v_add_u32_e32 v6, s4, v2
	v_mul_f32_e32 v5, 0x4f7ffffe, v5
	v_cvt_u32_f32_e32 v5, v5
	v_mul_lo_u32 v2, v4, v5
	v_mul_hi_u32 v2, v5, v2
	v_add_u32_e32 v2, v5, v2
	v_mul_hi_u32 v2, v6, v2
	v_mul_lo_u32 v4, v2, v3
	v_sub_u32_e32 v4, v6, v4
	v_add_u32_e32 v5, 1, v2
	v_cmp_ge_u32_e32 vcc, v4, v3
	s_nop 1
	v_cndmask_b32_e32 v2, v2, v5, vcc
	v_sub_u32_e32 v5, v4, v3
	v_cndmask_b32_e32 v4, v4, v5, vcc
	v_add_u32_e32 v5, 1, v2
	v_cmp_ge_u32_e32 vcc, v4, v3
	v_add_u32_e32 v4, 1, v6
	s_nop 0
	v_cndmask_b32_e32 v2, v2, v5, vcc
	v_mul_lo_u32 v5, v3, v2
	v_add_u32_e32 v3, v5, v3
	v_cmp_ne_u32_e32 vcc, v4, v3
	s_and_saveexec_b64 s[4:5], vcc
	s_xor_b64 s[4:5], exec, s[4:5]
	s_cbranch_execz .LBB0_675
	s_waitcnt lgkmcnt(0)
	buffer_inv sc1
	v_add_u32_e32 v7, 1, v2
	v_mul_lo_u32 v7, v7, v1
	v_mov_b32_e32 v8, 0x3400
	v_mov_b32_e32 v1, 0x2000
	global_load_dword v1, v8, s[90:91] sc1
	s_add_u32 s8, s2, 0x2400
	s_addc_u32 s9, s3, 0
	s_waitcnt vmcnt(0)
	v_cmp_lt_u32_e32 vcc, v1, v7
	s_and_saveexec_b64 s[6:7], vcc
	s_cbranch_execz .LBB0_674
	s_mov_b32 s20, 1
	s_mov_b64 s[10:11], 0
	v_mov_b32_e32 v1, 0
	s_branch .LBB0_665

; __device__ __forceinline__ unsigned xb_ld(unsigned* p)              { return __hip_atomic_load(p, __ATOMIC_RELAXED, __HIP_MEMORY_SCOPE_AGENT); }
; #define XB_SPIN(cond, bar) do { unsigned _sp = 0; while (cond) { __builtin_amdgcn_s_sleep(1); \
;     if ((++_sp & 255u) == 0u) { if (xb_ld(&(bar)[XB_TMO])) break; if (_sp > XB_SPIN_CAP) { atomicAdd(&(bar)[XB_TMO], 1u); break; } } } } while (0)
; __device__ __forceinline__ void xcd_barrier(const XcdBarrier& b) {
;     ...
;             XB_SPIN(xb_ld(&bar[XB_XGEN(b.x)]) == gen, bar);
.LBB0_667:
	global_load_dword v3, v8, s[90:91] sc1
	s_add_i32 s20, s20, 1
	s_mov_b64 s[16:17], -1
	s_waitcnt vmcnt(0)
	v_cmp_ge_u32_e32 vcc, v3, v7
	s_orn2_b64 s[14:15], vcc, exec
	s_branch .LBB0_664

; __device__ __forceinline__ unsigned xb_ld(unsigned* p)              { return __hip_atomic_load(p, __ATOMIC_RELAXED, __HIP_MEMORY_SCOPE_AGENT); }
; __device__ __forceinline__ unsigned xb_add(unsigned* p, unsigned v) { return __hip_atomic_fetch_add(p, v, __ATOMIC_RELAXED, __HIP_MEMORY_SCOPE_AGENT); }
; #define XB_SPIN(cond, bar) do { unsigned _sp = 0; while (cond) { __builtin_amdgcn_s_sleep(1); \
;     if ((++_sp & 255u) == 0u) { if (xb_ld(&(bar)[XB_TMO])) break; if (_sp > XB_SPIN_CAP) { atomicAdd(&(bar)[XB_TMO], 1u); break; } } } } while (0)
; __device__ __forceinline__ void xcd_barrier(const XcdBarrier& b) {
;     ...
;         const unsigned old = xb_add(&bar[XB_XSUB(b.x)], 1u);
;         const unsigned gen = old / nloc;
;         if (old + 1u == (gen + 1u) * nloc) {
;     ...
;         } else {
;             XB_SPIN(xb_ld(&bar[XB_XGEN(b.x)]) == gen, bar);
;             __builtin_amdgcn_fence(__ATOMIC_ACQUIRE, "agent");
.LBB0_1212:
	s_or_b64 exec, exec, s[8:9]
	v_cvt_f32_u32_e32 v5, v3
	s_waitcnt vmcnt(0)
	v_readfirstlane_b32 s6, v4
	v_sub_u32_e32 v4, 0, v3
	v_rcp_iflag_f32_e32 v5, v5
	v_add_u32_e32 v6, s6, v2
	v_mul_f32_e32 v5, 0x4f7ffffe, v5
	v_cvt_u32_f32_e32 v5, v5
	v_mul_lo_u32 v2, v4, v5
	v_mul_hi_u32 v2, v5, v2
	v_add_u32_e32 v2, v5, v2
	v_mul_hi_u32 v2, v6, v2
	v_mul_lo_u32 v4, v2, v3
	v_sub_u32_e32 v4, v6, v4
	v_add_u32_e32 v5, 1, v2
	v_cmp_ge_u32_e32 vcc, v4, v3
	s_nop 1
	v_cndmask_b32_e32 v2, v2, v5, vcc
	v_sub_u32_e32 v5, v4, v3
	v_cndmask_b32_e32 v4, v4, v5, vcc
	v_add_u32_e32 v5, 1, v2
	v_cmp_ge_u32_e32 vcc, v4, v3
	v_add_u32_e32 v4, 1, v6
	s_nop 0
	v_cndmask_b32_e32 v2, v2, v5, vcc
	v_mul_lo_u32 v5, v3, v2
	v_add_u32_e32 v3, v5, v3
	v_cmp_ne_u32_e32 vcc, v4, v3
	s_and_saveexec_b64 s[6:7], vcc
	s_xor_b64 s[6:7], exec, s[6:7]
	s_cbranch_execz .LBB0_1226
	s_waitcnt lgkmcnt(0)
	buffer_inv sc1
	v_add_u32_e32 v7, 1, v2
	v_mul_lo_u32 v7, v7, v1
	v_mov_b32_e32 v8, 0x3400
	v_mov_b32_e32 v1, 0x2000
	global_load_dword v1, v8, s[90:91] sc1
	s_add_u32 s10, s2, 0x2400
	s_addc_u32 s11, s3, 0
	s_waitcnt vmcnt(0)
	v_cmp_lt_u32_e32 vcc, v1, v7
	s_and_saveexec_b64 s[8:9], vcc
	s_cbranch_execz .LBB0_1225
	s_mov_b32 s22, 1
	s_mov_b64 s[12:13], 0
	v_mov_b32_e32 v1, 0
	s_branch .LBB0_1216

; __device__ __forceinline__ unsigned xb_ld(unsigned* p)              { return __hip_atomic_load(p, __ATOMIC_RELAXED, __HIP_MEMORY_SCOPE_AGENT); }
; #define XB_SPIN(cond, bar) do { unsigned _sp = 0; while (cond) { __builtin_amdgcn_s_sleep(1); \
;     if ((++_sp & 255u) == 0u) { if (xb_ld(&(bar)[XB_TMO])) break; if (_sp > XB_SPIN_CAP) { atomicAdd(&(bar)[XB_TMO], 1u); break; } } } } while (0)
; __device__ __forceinline__ void xcd_barrier(const XcdBarrier& b) {
;     ...
;             XB_SPIN(xb_ld(&bar[XB_XGEN(b.x)]) == gen, bar);
.LBB0_1442:
	global_load_dword v3, v8, s[90:91] sc1
	s_add_i32 s22, s22, 1
	s_mov_b64 s[28:29], -1
	s_waitcnt vmcnt(0)
	v_cmp_ge_u32_e32 vcc, v3, v7
	s_orn2_b64 s[26:27], vcc, exec
	s_branch .LBB0_1439

; __device__ __forceinline__ unsigned xb_ld(unsigned* p)              { return __hip_atomic_load(p, __ATOMIC_RELAXED, __HIP_MEMORY_SCOPE_AGENT); }
; __device__ __forceinline__ unsigned xb_add(unsigned* p, unsigned v) { return __hip_atomic_fetch_add(p, v, __ATOMIC_RELAXED, __HIP_MEMORY_SCOPE_AGENT); }
; #define XB_SPIN(cond, bar) do { unsigned _sp = 0; while (cond) { __builtin_amdgcn_s_sleep(1); \
;     if ((++_sp & 255u) == 0u) { if (xb_ld(&(bar)[XB_TMO])) break; if (_sp > XB_SPIN_CAP) { atomicAdd(&(bar)[XB_TMO], 1u); break; } } } } while (0)
; __device__ __forceinline__ void xcd_barrier(const XcdBarrier& b) {
;     ...
;         const unsigned old = xb_add(&bar[XB_XSUB(b.x)], 1u);
;         const unsigned gen = old / nloc;
;         if (old + 1u == (gen + 1u) * nloc) {
;     ...
;         } else {
;             XB_SPIN(xb_ld(&bar[XB_XGEN(b.x)]) == gen, bar);
;             __builtin_amdgcn_fence(__ATOMIC_ACQUIRE, "agent");
.LBB0_1743:
	s_or_b64 exec, exec, s[8:9]
	v_cvt_f32_u32_e32 v5, v3
	s_waitcnt vmcnt(0)
	v_readfirstlane_b32 s6, v4
	v_sub_u32_e32 v4, 0, v3
	v_rcp_iflag_f32_e32 v5, v5
	v_add_u32_e32 v6, s6, v2
	v_mul_f32_e32 v5, 0x4f7ffffe, v5
	v_cvt_u32_f32_e32 v5, v5
	v_mul_lo_u32 v2, v4, v5
	v_mul_hi_u32 v2, v5, v2
	v_add_u32_e32 v2, v5, v2
	v_mul_hi_u32 v2, v6, v2
	v_mul_lo_u32 v4, v2, v3
	v_sub_u32_e32 v4, v6, v4
	v_add_u32_e32 v5, 1, v2
	v_cmp_ge_u32_e32 vcc, v4, v3
	s_nop 1
	v_cndmask_b32_e32 v2, v2, v5, vcc
	v_sub_u32_e32 v5, v4, v3
	v_cndmask_b32_e32 v4, v4, v5, vcc
	v_add_u32_e32 v5, 1, v2
	v_cmp_ge_u32_e32 vcc, v4, v3
	v_add_u32_e32 v4, 1, v6
	s_nop 0
	v_cndmask_b32_e32 v2, v2, v5, vcc
	v_mul_lo_u32 v5, v3, v2
	v_add_u32_e32 v3, v5, v3
	v_cmp_ne_u32_e32 vcc, v4, v3
	s_and_saveexec_b64 s[6:7], vcc
	s_xor_b64 s[6:7], exec, s[6:7]
	s_cbranch_execz .LBB0_1757
	s_waitcnt lgkmcnt(0)
	buffer_inv sc1
	v_add_u32_e32 v7, 1, v2
	v_mul_lo_u32 v7, v7, v1
	v_mov_b32_e32 v8, 0x3400
	v_mov_b32_e32 v1, 0x2000
	global_load_dword v1, v8, s[90:91] sc1
	s_add_u32 s10, s2, 0x2400
	s_addc_u32 s11, s3, 0
	s_waitcnt vmcnt(0)
	v_cmp_lt_u32_e32 vcc, v1, v7
	s_and_saveexec_b64 s[8:9], vcc
	s_cbranch_execz .LBB0_1756
	s_mov_b32 s26, 1
	s_mov_b64 s[12:13], 0
	v_mov_b32_e32 v1, 0
	s_branch .LBB0_1747

; __device__ __forceinline__ unsigned xb_ld(unsigned* p)              { return __hip_atomic_load(p, __ATOMIC_RELAXED, __HIP_MEMORY_SCOPE_AGENT); }
; #define XB_SPIN(cond, bar) do { unsigned _sp = 0; while (cond) { __builtin_amdgcn_s_sleep(1); \
;     if ((++_sp & 255u) == 0u) { if (xb_ld(&(bar)[XB_TMO])) break; if (_sp > XB_SPIN_CAP) { atomicAdd(&(bar)[XB_TMO], 1u); break; } } } } while (0)
; __device__ __forceinline__ void xcd_barrier(const XcdBarrier& b) {
;     ...
;             XB_SPIN(xb_ld(&bar[XB_XGEN(b.x)]) == gen, bar);
.LBB0_1749:
	global_load_dword v3, v8, s[90:91] sc1
	s_add_i32 s26, s26, 1
	s_mov_b64 s[22:23], -1
	s_waitcnt vmcnt(0)
	v_cmp_ge_u32_e32 vcc, v3, v7
	s_orn2_b64 s[20:21], vcc, exec
	s_branch .LBB0_1746

; __device__ __forceinline__ unsigned xb_ld(unsigned* p)              { return __hip_atomic_load(p, __ATOMIC_RELAXED, __HIP_MEMORY_SCOPE_AGENT); }
; __device__ __forceinline__ unsigned xb_add(unsigned* p, unsigned v) { return __hip_atomic_fetch_add(p, v, __ATOMIC_RELAXED, __HIP_MEMORY_SCOPE_AGENT); }
; #define XB_SPIN(cond, bar) do { unsigned _sp = 0; while (cond) { __builtin_amdgcn_s_sleep(1); \
;     if ((++_sp & 255u) == 0u) { if (xb_ld(&(bar)[XB_TMO])) break; if (_sp > XB_SPIN_CAP) { atomicAdd(&(bar)[XB_TMO], 1u); break; } } } } while (0)
; __device__ __forceinline__ void xcd_barrier(const XcdBarrier& b) {
;     ...
;         const unsigned old = xb_add(&bar[XB_XSUB(b.x)], 1u);
;         const unsigned gen = old / nloc;
;         if (old + 1u == (gen + 1u) * nloc) {
;     ...
;         } else {
;             XB_SPIN(xb_ld(&bar[XB_XGEN(b.x)]) == gen, bar);
;             __builtin_amdgcn_fence(__ATOMIC_ACQUIRE, "agent");
.LBB0_1826:
	s_or_b64 exec, exec, s[8:9]
	v_cvt_f32_u32_e32 v5, v3
	s_waitcnt vmcnt(0)
	v_readfirstlane_b32 s6, v4
	v_sub_u32_e32 v4, 0, v3
	v_rcp_iflag_f32_e32 v5, v5
	v_add_u32_e32 v6, s6, v2
	v_mul_f32_e32 v5, 0x4f7ffffe, v5
	v_cvt_u32_f32_e32 v5, v5
	v_mul_lo_u32 v2, v4, v5
	v_mul_hi_u32 v2, v5, v2
	v_add_u32_e32 v2, v5, v2
	v_mul_hi_u32 v2, v6, v2
	v_mul_lo_u32 v4, v2, v3
	v_sub_u32_e32 v4, v6, v4
	v_add_u32_e32 v5, 1, v2
	v_cmp_ge_u32_e32 vcc, v4, v3
	s_nop 1
	v_cndmask_b32_e32 v2, v2, v5, vcc
	v_sub_u32_e32 v5, v4, v3
	v_cndmask_b32_e32 v4, v4, v5, vcc
	v_add_u32_e32 v5, 1, v2
	v_cmp_ge_u32_e32 vcc, v4, v3
	v_add_u32_e32 v4, 1, v6
	s_nop 0
	v_cndmask_b32_e32 v2, v2, v5, vcc
	v_mul_lo_u32 v5, v3, v2
	v_add_u32_e32 v3, v5, v3
	v_cmp_ne_u32_e32 vcc, v4, v3
	s_and_saveexec_b64 s[6:7], vcc
	s_xor_b64 s[6:7], exec, s[6:7]
	s_cbranch_execz .LBB0_1840
	s_waitcnt lgkmcnt(0)
	buffer_inv sc1
	v_add_u32_e32 v7, 1, v2
	v_mul_lo_u32 v7, v7, v1
	v_mov_b32_e32 v8, 0x3400
	v_mov_b32_e32 v1, 0x2000
	global_load_dword v1, v8, s[90:91] sc1
	s_add_u32 s10, s2, 0x2400
	s_addc_u32 s11, s3, 0
	s_waitcnt vmcnt(0)
	v_cmp_lt_u32_e32 vcc, v1, v7
	s_and_saveexec_b64 s[8:9], vcc
	s_cbranch_execz .LBB0_1839
	s_mov_b32 s24, 1
	s_mov_b64 s[12:13], 0
	v_mov_b32_e32 v1, 0
	s_branch .LBB0_1830

; __device__ __forceinline__ unsigned xb_ld(unsigned* p)              { return __hip_atomic_load(p, __ATOMIC_RELAXED, __HIP_MEMORY_SCOPE_AGENT); }
; #define XB_SPIN(cond, bar) do { unsigned _sp = 0; while (cond) { __builtin_amdgcn_s_sleep(1); \
;     if ((++_sp & 255u) == 0u) { if (xb_ld(&(bar)[XB_TMO])) break; if (_sp > XB_SPIN_CAP) { atomicAdd(&(bar)[XB_TMO], 1u); break; } } } } while (0)
; __device__ __forceinline__ void xcd_barrier(const XcdBarrier& b) {
;     ...
;             XB_SPIN(xb_ld(&bar[XB_XGEN(b.x)]) == gen, bar);
.LBB0_1832:
	global_load_dword v3, v8, s[90:91] sc1
	s_add_i32 s24, s24, 1
	s_mov_b64 s[20:21], -1
	s_waitcnt vmcnt(0)
	v_cmp_ge_u32_e32 vcc, v3, v7
	s_orn2_b64 s[18:19], vcc, exec
	s_branch .LBB0_1829
